# m8 + converter-workgroup count of the gate/up GEMM phase chosen from the tile count at run time (as many as fit without adding a GEMM round), XP5 32, N_DEFER 64
# speedup vs baseline: 1.0162x; 1.0005x over previous
; #define LAS __attribute__((address_space(3)))
; __global__ void __launch_bounds__(NTHREADS, 2) fwd(Params p) {
;     ...
;         ntiles = __builtin_amdgcn_readfirstlane(cnt[NE]); }
;     {
;         pg8::Gemm g{(const bf16_t*)p.xb, (const bf16_t*)p.wt_gu, ND / 2, ND / 2, ND / 2};
;         MoeOrder S{G, bid, 2 * DFF / 256, ntiles, (const LAS unsigned*)(lds + LDS_MISC), (size_t)256 * ND, (size_t)(2 * DFF) * ND, (size_t)256 * ND}; S.ncv = NCV;
;         if (bid < NCV) conv_queue(p, lds, wave, CW_CONV4, N_GU + XP5, N_GU + N_DN - N_DEFER, LDS_MISC + 1024);
.LBB0_1244:
	s_or_b64 exec, exec, s[4:5]
	s_add_i32 s0, 0, 0x20580
	v_mov_b32_e32 v0, s0
	s_waitcnt lgkmcnt(0)
	s_barrier
	ds_read_b32 v0, v0
	v_readlane_b32 s0, v254, 3
	s_cmp_gt_i32 s0, 23
	s_cselect_b64 s[6:7], -1, 0
	s_mov_b32 s5, 0
	s_waitcnt lgkmcnt(0)
	v_readfirstlane_b32 s3, v0
	v_readlane_b32 s1, v254, 4
	s_lshl_b32 s100, s3, 4
	s_mov_b32 s99, 1
.Lncv_r:
	s_mul_i32 s101, s99, 0xe8
	s_cmp_lt_u32 s101, s100
	s_cbranch_scc0 .Lncv_r_done
	s_add_u32 s99, s99, 1
	s_branch .Lncv_r
.Lncv_r_done:
	s_mov_b32 s98, 0xc0
.Lncv_p:
	s_mul_i32 s101, s98, s99
	s_cmp_lt_u32 s101, s100
	s_cbranch_scc0 .Lncv_p_done
	s_add_u32 s98, s98, 1
	s_cmp_lt_u32 s98, 0xe8
	s_cbranch_scc1 .Lncv_p
.Lncv_p_done:
	s_sub_u32 s98, 0x100, s98
	s_cmp_ge_i32 s0, s98
	s_cselect_b64 s[6:7], -1, 0
	s_and_b64 vcc, exec, s[6:7]
	s_cbranch_vccnz .LBB0_1257
	v_mbcnt_lo_u32_b32 v1, -1, 0
	v_mbcnt_hi_u32_b32 v1, -1, v1
	v_readlane_b32 s2, v255, 30
	v_and_b32_e32 v2, 63, v1
	v_add_u32_e32 v3, s91, v1
	v_lshlrev_b32_e32 v0, 2, v2
	v_lshl_add_u32 v6, v2, 9, 0
	v_bitop3_b32 v2, v1, s2, 7 bitop3:0x6c
	v_cmp_eq_u32_e64 s[0:1], 0, v3
	v_lshlrev_b32_e32 v7, 4, v2
	v_ashrrev_i32_e32 v2, 3, v3
	v_lshrrev_b32_e32 v3, 5, v3
	v_xor_b32_e32 v3, v3, v1
	v_lshlrev_b32_e32 v3, 4, v3
	v_add_u32_e32 v4, 64, v2
	v_and_b32_e32 v3, 0x70, v3
	v_ashrrev_i32_e32 v5, 31, v4
	v_add_u32_e32 v8, 0, v3
	v_lshlrev_b32_e32 v1, 4, v1
	v_ashrrev_i32_e32 v3, 31, v2
	v_lshlrev_b32_e32 v9, 7, v4
	v_lshlrev_b64 v[142:143], 11, v[4:5]
	v_add_u32_e32 v4, 0x80, v2
	v_readlane_b32 s16, v254, 5
	v_and_b32_e32 v138, 0x70, v1
	v_lshlrev_b32_e32 v1, 7, v2
	v_lshlrev_b64 v[140:141], 11, v[2:3]
	v_ashrrev_i32_e32 v5, 31, v4
	v_add_u32_e32 v2, 0xc0, v2
	v_readlane_b32 s17, v254, 6
	s_add_u32 s8, s16, 0x20e0
	v_mov_b32_e32 v137, 0
	v_lshlrev_b32_e32 v10, 7, v4
	v_lshlrev_b64 v[144:145], 11, v[4:5]
	v_lshlrev_b32_e32 v4, 7, v2
	v_ashrrev_i32_e32 v3, 31, v2
	s_addc_u32 s9, s17, 0
	s_add_i32 s13, 0, 0x20400
	v_mov_b32_e32 v139, v137
	v_lshlrev_b64 v[146:147], 11, v[2:3]
	v_mov_b32_e32 v204, s13
	s_movk_i32 s60, 0x4000
	s_mov_b32 s61, 0x8000
	s_mov_b32 s62, 0xc000
	s_mov_b32 s63, 0x10000
	s_mov_b32 s64, 0x14000
	s_mov_b32 s65, 0x18000
	s_mov_b32 s66, 0x1c000
	v_add_u32_e32 v205, v6, v7
	v_add_u32_e32 v206, v8, v1
	v_add_u32_e32 v207, v8, v9
	v_add_u32_e32 v208, v8, v10
	v_add_u32_e32 v209, v8, v4
	s_mov_b64 s[10:11], 0x80000
	s_mov_b64 s[38:39], 0x100000
	s_movk_i32 s67, 0x1000
	s_movk_i32 s68, 0x5000
	s_mov_b32 s69, 0x9000
	s_mov_b32 s70, 0xd000
	s_mov_b32 s71, 0x11000
	s_mov_b32 s72, 0x15000
	s_mov_b32 s73, 0x19000
	s_mov_b32 s74, 0x1d000
	s_mov_b64 s[40:41], 0x180000
	s_mov_b64 s[42:43], 0x200000
	s_mov_b64 s[44:45], 0x280000
	s_mov_b64 s[46:47], 0x300000
	s_mov_b64 s[48:49], 0x380000
	v_lshlrev_b32_e32 v136, 2, v0
	v_readlane_b32 s18, v254, 7
	v_readlane_b32 s19, v254, 8
	v_readlane_b32 s20, v254, 9
	v_readlane_b32 s21, v254, 10
	v_readlane_b32 s22, v254, 11
	v_readlane_b32 s23, v254, 12
	v_readlane_b32 s24, v254, 13
	v_readlane_b32 s25, v254, 14
	v_readlane_b32 s26, v254, 15
	v_readlane_b32 s27, v254, 16
	v_readlane_b32 s28, v254, 17
	v_readlane_b32 s29, v254, 18
	v_readlane_b32 s30, v254, 19
	v_readlane_b32 s31, v254, 20
	s_branch .LBB0_1248

; #define LAS __attribute__((address_space(3)))
; template <class Epi, class Sched, bool FP8 = false>
; __device__ __forceinline__ void gemm_phase(LAS unsigned char* lds, const Gemm g, const Sched& S, const Epi& E, const int wave) {
;     const int tid = phase_tid(wave);
;     const int wid = __builtin_amdgcn_readfirstlane(tid >> 6), lane = tid & 63, wr = wid >> 2, wc = wid & 3, fr = lane & 15, fq = lane >> 4;
;     const int K = g.K, nt = K / BK;
;     unsigned voffA, voffB;
;     {   int R, C; stage_rc(tid * 16, R, C); const int Rb = Epi::PERM ? ((R & ~31) + perm32(R & 31)) : R;
;         voffA = (unsigned)(R * g.lda + C) * 2u; voffB = (unsigned)(Rb * g.ldb + C) * 2u; }
;     const unsigned pieceA = 64u * (unsigned)g.lda * 2u, pieceB = 64u * (unsigned)g.ldb * 2u;
;     const unsigned kstep = (unsigned)(BK * 2);
;     const unsigned hstepA = (unsigned)HALF * g.lda * 2u, hstepB = (unsigned)HALF * g.ldb * 2u;
;     const __amdgpu_buffer_rsrc_t rsA = __builtin_amdgcn_make_buffer_rsrc((void*)g.A, (short)0, -1, 0x00020000), rsB = __builtin_amdgcn_make_buffer_rsrc((void*)g.Bt, (short)0, -1, 0x00020000);
;     const unsigned ldsw = (unsigned)wid * 1024u;
;     const int aoff = lds_byte(wr * 64 + fr, fq * 8), boff = lds_byte(wc * 32 + fr, fq * 8);
;     ...
;     Unit cur, nxt; int ui = 0;
;     if (!S.next(0, cur)) return;
;     f32x4 acc[2][2][4][2];
; #pragma unroll
;     for (int a = 0; a < 2; ++a)
; #pragma unroll
;         for (int b = 0; b < 2; ++b)
; #pragma unroll
;             for (int m = 0; m < 4; ++m)
; #pragma unroll
;                 for (int n = 0; n < 2; ++n) acc[a][b][m][n] = (f32x4){0.f, 0.f, 0.f, 0.f};
;     bf16x8 At[4][2], B0[2][2], B1[2][2];
;     unsigned cA = cur.aoff, cB = cur.boff;
;     PG8_STAGE(PG8_SB(0, 0), rsB, cB, voffB); PG8_STAGE(PG8_SA(0, 0), rsA, cA, voffA); PG8_STAGE(PG8_SB(0, 1), rsB, cB + hstepB, voffB); PG8_STAGE(PG8_SA(0, 1), rsA, cA + hstepA, voffA);
;     if (wr == 1) PG8_BAR;
;     PG8_WAIT_V(4); PG8_BAR;
;     __device__ bool next(int i, Unit& u) const {
;         const int L = i * (G - ncv) + (c - ncv); if (c < ncv || L >= ntiles * nN) return false;
;         u.pm = __builtin_amdgcn_readfirstlane((int)tile_e[L / nN]); u.pn = L % nN; u.e = u.pm >> 5;
;         u.aoff = (unsigned)((size_t)u.pm * a_tile); u.boff = (unsigned)((size_t)u.e * b_expert + (size_t)u.pn * b_tile); return true;
.LBB0_1257:
	v_mbcnt_lo_u32_b32 v0, -1, 0
	v_mbcnt_hi_u32_b32 v0, -1, v0
	s_mov_b32 s4, s86
	v_add_u32_e32 v1, s91, v0
	s_mov_b32 s5, s87
	s_andn2_b64 vcc, exec, s[6:7]
	v_readfirstlane_b32 s1, v1
	v_readlane_b32 s86, v254, 3
	v_readlane_b32 s87, v254, 4
	s_cbranch_vccnz .LBB0_1270
	s_sub_i32 s13, s86, s98
	s_lshl_b32 s33, s3, 4
	s_cmp_ge_i32 s13, s33
	s_cbranch_scc1 .LBB0_1270
	v_ashrrev_i32_e32 v3, 31, v1
	v_lshrrev_b32_e32 v3, 26, v3
	v_lshlrev_b32_e32 v2, 4, v1
	v_add_u32_e32 v3, v1, v3
	v_bfe_i32 v1, v1, 27, 1
	v_lshrrev_b32_e32 v1, 22, v1
	v_add_u32_e32 v1, v2, v1
	v_and_b32_e32 v1, 0xfffffc00, v1
	v_sub_u32_e32 v1, v2, v1
	v_lshrrev_b32_e32 v2, 4, v1
	v_bitop3_b32 v1, v2, v1, 32 bitop3:0x6c
	v_ashrrev_i32_e32 v4, 31, v1
	v_ashrrev_i32_e32 v3, 6, v3
	v_lshrrev_b32_e32 v4, 26, v4
	v_lshlrev_b32_e32 v2, 3, v3
	v_add_u32_e32 v4, v1, v4
	v_and_b32_e32 v2, -16, v2
	v_ashrrev_i32_e32 v5, 6, v4
	v_add_u32_e32 v2, v5, v2
	v_and_b32_e32 v4, 0xc0, v4
	v_and_b32_e32 v5, 3, v5
	s_mov_b32 s2, 0x1fffe0
	v_sub_u32_e32 v1, v1, v4
	v_mov_b32_e32 v4, 1
	v_and_or_b32 v5, v2, s2, v5
	s_lshr_b32 s2, s13, 2
	v_lshlrev_b32_e32 v3, 5, v3
	v_ashrrev_i16_sdwa v1, v4, sext(v1) dst_sel:DWORD dst_unused:UNUSED_PAD src0_sel:DWORD src1_sel:BYTE_0
	v_lshlrev_b32_e32 v4, 1, v2
	v_lshrrev_b32_e32 v6, 2, v2
	s_and_b32 s2, s2, 0x3ffffffc
	v_and_b32_e32 v3, 32, v3
	v_bfe_i32 v1, v1, 0, 16
	v_and_b32_e32 v4, 24, v4
	v_and_b32_e32 v6, 4, v6
	s_add_i32 s2, s2, 0
	v_or3_b32 v4, v5, v6, v4
	v_add_lshl_u32 v1, v3, v1, 1
	s_add_i32 s2, s2, 0x20000
	v_lshl_add_u32 v138, v2, 11, v1
	v_lshl_add_u32 v139, v4, 11, v1
	v_mov_b32_e32 v1, s2
	ds_read_b32 v1, v1
	s_ashr_i32 s0, s1, 6
	s_and_b32 s71, s13, 15
	s_lshl_b32 s6, s0, 10
	s_lshl_b32 s34, s71, 19
	s_waitcnt lgkmcnt(0)
	v_readfirstlane_b32 s72, v1
	s_ashr_i32 s38, s72, 5
	s_lshl_b32 s7, s38, 23
	s_or_b32 s75, s7, s34
	s_add_i32 s34, s6, 0
	s_mov_b32 s87, 0x20000
	s_mov_b32 s86, -1
	s_add_i32 s35, s34, 0x10000
	s_and_b32 s9, s55, 0xffff
	s_mov_b32 s8, s54
	s_mov_b32 s10, s86
	s_mov_b32 s11, s87
	s_mov_b32 m0, s35
	s_add_i32 s40, s34, 0x12000
	buffer_load_dwordx4 v139, s[8:11], s75 offen lds
	s_or_b32 s6, s75, 0x20000
	s_mov_b32 m0, s40
	s_and_b32 s85, s85, 0xffff
	s_lshl_b32 s2, s72, 19
	buffer_load_dwordx4 v139, s[8:11], s6 offen lds
	s_mov_b32 m0, s34
	s_add_i32 s41, s34, 0x2000
	buffer_load_dwordx4 v138, s[84:87], s2 offen lds
	s_or_b32 s6, s2, 0x20000
	s_mov_b32 m0, s41
	s_add_i32 s42, s34, 0x14000
	buffer_load_dwordx4 v138, s[84:87], s6 offen lds
	s_or_b32 s6, s75, 0x40000
	s_mov_b32 m0, s42
	s_add_i32 s43, s34, 0x16000
	buffer_load_dwordx4 v139, s[8:11], s6 offen lds
	s_or_b32 s6, s75, 0x60000
	s_mov_b32 m0, s43
	s_add_i32 s44, s34, 0x4000
	buffer_load_dwordx4 v139, s[8:11], s6 offen lds
	s_or_b32 s6, s2, 0x40000
	s_mov_b32 m0, s44
	s_add_i32 s45, s34, 0x6000
	buffer_load_dwordx4 v138, s[84:87], s6 offen lds
	s_or_b32 s6, s2, 0x60000
	s_mov_b32 m0, s45
	s_mov_b32 s46, 0
	buffer_load_dwordx4 v138, s[84:87], s6 offen lds
	s_ashr_i32 s6, s1, 8
	s_cmp_lg_u32 s6, 1
	s_cbranch_scc1 .LBB0_1261
	s_barrier
.LBB0_1261:
	s_add_i32 s47, s34, 0x18000
	s_or_b32 s7, s75, 0x80
	s_mov_b32 s8, s54
	s_mov_b32 s10, s86
	s_mov_b32 s11, s87
	s_mov_b32 m0, s47
	s_add_i32 s48, s34, 0x1a000
	s_waitcnt vmcnt(4)
	s_barrier
	buffer_load_dwordx4 v139, s[8:11], s7 offen lds
	s_or_b32 s7, s75, 0x20080
	s_mov_b32 m0, s48
	s_add_i32 s49, s34, 0x8000
	buffer_load_dwordx4 v139, s[8:11], s7 offen lds
	s_or_b32 s7, s2, 0x80
	s_mov_b32 m0, s49
	s_add_i32 s50, s34, 0xa000
	buffer_load_dwordx4 v138, s[84:87], s7 offen lds
	s_or_b32 s7, s2, 0x20080
	s_mov_b32 m0, s50
	s_add_i32 s51, s34, 0x1c000
	buffer_load_dwordx4 v138, s[84:87], s7 offen lds
	s_or_b32 s7, s75, 0x40080
	s_mov_b32 m0, s51
	s_add_i32 s52, s34, 0x1e000
	buffer_load_dwordx4 v139, s[8:11], s7 offen lds
	s_or_b32 s7, s75, 0x60080
	s_mov_b32 m0, s52
	s_and_b32 s0, s0, 3
	buffer_load_dwordx4 v139, s[8:11], s7 offen lds
	v_and_b32_e32 v1, 48, v0
	v_lshlrev_b32_e32 v2, 6, v0
	s_movk_i32 s8, 0x3c0
	v_lshlrev_b32_e32 v0, 2, v0
	s_lshl_b32 s53, s6, 6
	s_lshl_b32 s7, s6, 13
	v_and_or_b32 v1, v2, s8, v1
	v_and_b32_e32 v0, 32, v0
	s_lshl_b32 s8, s0, 12
	s_mulk_i32 s6, 0x2400
	v_bitop3_b32 v2, v1, s7, v0 bitop3:0xde
	v_bitop3_b32 v0, v1, s8, v0 bitop3:0xde
	s_waitcnt vmcnt(6)
	s_add_i32 s62, s6, 0
	s_lshl_b32 s7, s0, 5
	s_lshl_b32 s8, s0, 4
	s_add_i32 s62, s62, 0x20800
	v_add_u32_e32 v0, 0, v0
	s_add_i32 s58, s34, 0xc000
	s_lshl_b32 s59, s0, 6
	s_add_i32 s60, s34, 0xe000
	s_sub_i32 s61, s89, s98
	s_add_i32 s63, s62, s8
	v_add_u32_e32 v140, 0x10000, v0
	v_add_u32_e32 v141, 0, v2
	v_mov_b32_e32 v142, 0x7f7f7f7f
	v_add_u32_e32 v143, 0x14000, v0
	v_add_u32_e32 v144, 0x18000, v0
	v_add_u32_e32 v145, 0x1c000, v0
	s_lshl_b32 s64, s7, 2
	v_mov_b32_e32 v137, 0
	s_mov_b32 s0, 0x3c800000
	s_mov_b32 s65, 0xc0e00000
	v_mov_b32_e32 v146, 0x40e00000
	s_barrier

; #define LAS __attribute__((address_space(3)))
; __global__ void __launch_bounds__(NTHREADS, 2) fwd(Params p) {
;     extern __shared__ __attribute__((aligned(16))) unsigned char shm[];
;     LAS unsigned char* lds = (LAS unsigned char*)shm;
;     const int bid = blockIdx.x, G = gridDim.x;
;     const int wave = __builtin_amdgcn_readfirstlane(threadIdx.x >> 6);
	.amdhsa_kernel _Z3fwd6Params
		.amdhsa_group_segment_fixed_size 0
		.amdhsa_private_segment_fixed_size 0
		.amdhsa_kernarg_size 728
		.amdhsa_user_sgpr_count 2
		.amdhsa_user_sgpr_dispatch_ptr 0
		.amdhsa_user_sgpr_queue_ptr 0
		.amdhsa_user_sgpr_kernarg_segment_ptr 1
		.amdhsa_user_sgpr_dispatch_id 0
		.amdhsa_user_sgpr_kernarg_preload_length 0
		.amdhsa_user_sgpr_kernarg_preload_offset 0
		.amdhsa_user_sgpr_private_segment_size 0
		.amdhsa_uses_dynamic_stack 0
		.amdhsa_enable_private_segment 0
		.amdhsa_system_sgpr_workgroup_id_x 1
		.amdhsa_system_sgpr_workgroup_id_y 0
		.amdhsa_system_sgpr_workgroup_id_z 0
		.amdhsa_system_sgpr_workgroup_info 0
		.amdhsa_system_vgpr_workitem_id 0
		.amdhsa_next_free_vgpr 256
		.amdhsa_next_free_sgpr 102
		.amdhsa_accum_offset 256
		.amdhsa_reserve_vcc 1
		.amdhsa_float_round_mode_32 0
		.amdhsa_float_round_mode_16_64 0
		.amdhsa_float_denorm_mode_32 3
		.amdhsa_float_denorm_mode_16_64 3
		.amdhsa_dx10_clamp 1
		.amdhsa_ieee_mode 1
		.amdhsa_fp16_overflow 0
		.amdhsa_tg_split 0
		.amdhsa_exception_fp_ieee_invalid_op 0
		.amdhsa_exception_fp_denorm_src 0
		.amdhsa_exception_fp_ieee_div_zero 0
		.amdhsa_exception_fp_ieee_overflow 0
		.amdhsa_exception_fp_ieee_underflow 0
		.amdhsa_exception_fp_ieee_inexact 0
		.amdhsa_exception_int_div_zero 0
	.end_amdhsa_kernel

; #define LAS __attribute__((address_space(3)))
; __global__ void __launch_bounds__(NTHREADS, 2) fwd(Params p) {
;     extern __shared__ __attribute__((aligned(16))) unsigned char shm[];
;     LAS unsigned char* lds = (LAS unsigned char*)shm;
;     const int bid = blockIdx.x, G = gridDim.x;
;     const int wave = __builtin_amdgcn_readfirstlane(threadIdx.x >> 6);
amdhsa.kernels:
  - .agpr_count:     0
    .args:
      - .offset:         0
        .size:           472
        .value_kind:     by_value
      - .offset:         472
        .size:           4
        .value_kind:     hidden_block_count_x
      - .offset:         476
        .size:           4
        .value_kind:     hidden_block_count_y
      - .offset:         480
        .size:           4
        .value_kind:     hidden_block_count_z
      - .offset:         484
        .size:           2
        .value_kind:     hidden_group_size_x
      - .offset:         486
        .size:           2
        .value_kind:     hidden_group_size_y
      - .offset:         488
        .size:           2
        .value_kind:     hidden_group_size_z
      - .offset:         490
        .size:           2
        .value_kind:     hidden_remainder_x
      - .offset:         492
        .size:           2
        .value_kind:     hidden_remainder_y
      - .offset:         494
        .size:           2
        .value_kind:     hidden_remainder_z
      - .offset:         512
        .size:           8
        .value_kind:     hidden_global_offset_x
      - .offset:         520
        .size:           8
        .value_kind:     hidden_global_offset_y
      - .offset:         528
        .size:           8
        .value_kind:     hidden_global_offset_z
      - .offset:         536
        .size:           2
        .value_kind:     hidden_grid_dims
      - .offset:         592
        .size:           4
        .value_kind:     hidden_dynamic_lds_size
    .group_segment_fixed_size: 0
    .kernarg_segment_align: 8
    .kernarg_segment_size: 728
    .language:       OpenCL C
    .language_version:
      - 2
      - 0
    .max_flat_workgroup_size: 512
    .name:           _Z3fwd6Params
    .private_segment_fixed_size: 0
    .sgpr_count:     108
    .sgpr_spill_count: 119
    .symbol:         _Z3fwd6Params.kd
    .uniform_work_group_size: 1
    .uses_dynamic_stack: false
    .vgpr_count:     256
    .vgpr_spill_count: 0
    .wavefront_size: 64
